# baseline (speedup 1.0000x reference)
_Z9qsim_mainPKDF16_PK15HIP_vector_typeIfLj2EEPf:
	s_cmpk_gt_i32 s2, 0x3ff
	s_cbranch_scc1 .LBB1_11
	s_load_dwordx4 s[8:11], s[0:1], 0x0
	s_load_dwordx2 s[4:5], s[0:1], 0x10
	s_mul_i32 s1, s2, 56
	s_mul_hi_i32 s0, s2, 56
	v_mbcnt_lo_u32_b32 v2, -1, 0
	s_waitcnt lgkmcnt(0)
	s_add_u32 s6, s8, 0x20000
	s_addc_u32 s7, s9, 0
	s_add_u32 s20, s8, 0x80000
	s_addc_u32 s21, s9, 0
	s_add_u32 s12, s8, 0x38000
	s_addc_u32 s13, s9, 0
	s_add_i32 s22, s2, 0xfffffe00
	s_add_u32 s14, s4, s1
	s_addc_u32 s15, s5, s0
	s_mul_hi_i32 s0, s2, 0xa00
	s_mulk_i32 s2, 0xa00
	v_mbcnt_hi_u32_b32 v161, -1, v2
	s_add_u32 s10, s10, s2
	v_and_b32_e32 v2, 64, v161
	s_addc_u32 s11, s11, s0
	v_mov_b32_e32 v155, 0
	s_movk_i32 s23, 0x1000
	s_mov_b64 s[16:17], 0x28000
	v_mov_b32_e32 v1, 0x10000
	s_movk_i32 s24, 0x100
	v_mov_b32_e32 v158, 0x60
	v_mov_b32_e32 v159, 0x280
	v_mov_b32_e32 v160, 0x1280
	s_mov_b64 s[18:19], 0x40000
	s_mov_b32 s25, 0x40000
	v_xor_b32_e32 v162, 32, v161
	v_add_u32_e32 v163, 64, v2
	v_xor_b32_e32 v164, 16, v161
	v_mov_b32_e32 v165, 0x10a00
	s_getreg_b32 s35, hwreg(HW_REG_LDS_ALLOC, 0, 8)
	s_cmp_eq_u32 s35, 0
	s_cbranch_scc1 .Lprio0_old
	s_setprio 1
.Lprio0_old:
	v_and_b32_e32 v2, 63, v0
	v_lshlrev_b32_e32 v2, 4, v2
	v_add_u32_e32 v3, 0x1000, v2
	global_load_dwordx4 v[222:225], v2, s[6:7]
	global_load_dwordx4 v[226:229], v2, s[6:7] offset:1024
	global_load_dwordx4 v[230:233], v2, s[6:7] offset:2048
	global_load_dwordx4 v[234:237], v2, s[6:7] offset:3072
	global_load_dwordx4 v[238:241], v3, s[6:7]
	global_load_dwordx4 v[242:245], v3, s[6:7] offset:1024
	global_load_dwordx4 v[246:249], v3, s[6:7] offset:2048
	global_load_dwordx4 v[250:253], v3, s[6:7] offset:3072
	s_nop 0
	s_nop 0
	s_branch .LBB1_3

.Lskip_stage0:
	s_ashr_i32 s2, s4, 6
	s_lshl_b32 s3, s2, 3
	s_and_b32 s5, s3, 8
	s_bfe_u32 s26, s2, 0x10001
	s_or_b32 s5, s26, s5
	s_lshl_b32 s26, s2, 9
	s_and_b32 s26, s26, 0x400
	s_lshl_b32 s5, s5, 4
	s_or_b32 s28, s5, s26
	v_lshrrev_b32_e32 v182, 5, v167
	v_bfe_u32 v2, v156, 4, 1
	v_bitop3_b32 v3, v182, v156, 1 bitop3:0x78
	v_lshlrev_b32_e32 v154, 2, v182
	v_xor_b32_e32 v3, v3, v2
	v_bitop3_b32 v4, v154, v156, 4 bitop3:0x78
	v_and_b32_e32 v5, 10, v156
	v_or3_b32 v3, v5, v4, v3
	s_lshl_b32 s5, s2, 4
	v_lshlrev_b32_e32 v3, 4, v3
	s_lshl_b32 s3, s2, 13
	s_and_b32 s29, s5, 16
	v_lshlrev_b32_e32 v170, 8, v182
	v_lshl_or_b32 v171, v2, 10, v3
	s_or_b32 s26, s29, s3
	v_bitop3_b32 v179, v171, s26, v170 bitop3:0x36
	s_or_b32 s5, s26, 0x280
	v_bitop3_b32 v178, v171, s5, v170 bitop3:0x36
	s_or_b32 s30, s3, 0x800
	s_or_b32 s33, s3, 0x1000
	s_or_b32 s29, s29, 64
	s_or_b32 s34, s29, s33
	v_bitop3_b32 v180, v171, s34, v170 bitop3:0x36
	s_or_b32 s29, s3, s29
	s_or_b32 s29, s29, 0x1280
	s_and_b32 s5, s2, 1
	s_lshl_b32 s31, s5, 4
	s_or_b32 s2, s31, s3
	v_bitop3_b32 v173, v171, s2, v170 bitop3:0x36
	v_bitop3_b32 v34, v156, 31, v156 bitop3:0xc
	v_lshrrev_b32_e32 v35, 4, v34
	v_bitop3_b32 v36, v34, v182, 1 bitop3:0x6c
	v_xor_b32_e32 v36, v36, v35
	v_bitop3_b32 v34, v34, v154, 4 bitop3:0x6c
	v_bitop3_b32 v37, v156, 10, 31 bitop3:8
	v_or3_b32 v34, v37, v34, v36
	v_lshlrev_b32_e32 v35, 10, v35
	v_lshlrev_b32_e32 v34, 4, v34
	v_or3_b32 v154, v35, v34, v170
	v_bitop3_b32 v172, s2, v154, v159 bitop3:0x36
	v_bitop3_b32 v176, v171, s29, v170 bitop3:0x36
	s_or_b32 s29, s31, s30
	s_or_b32 s29, s29, 0xa0
	v_bitop3_b32 v175, v171, s29, v170 bitop3:0x36
	s_or_b32 s29, s2, 0xaa0
	s_xor_b32 s29, s29, 0x80
	v_xor_b32_e32 v174, s29, v154
	s_or_b32 s29, s26, 0x18e0
	v_bitop3_b32 v181, v171, s29, v170 bitop3:0x36
	s_or_b32 s29, s26, 0x1a60
	v_bitop3_b32 v177, v171, s29, v170 bitop3:0x36
	s_or_b32 s29, s31, 64
	s_or_b32 s3, s3, s29
	s_mov_b32 s41, s3
	s_or_b32 s29, s29, s33
	s_mov_b32 s40, s29
	s_or_b32 s3, s2, 0x18e0
	s_mov_b32 s42, s3
	s_or_b32 s2, s2, 0x1ae0
	s_xor_b32 s2, s2, 0x80
	s_mov_b32 s43, s2
	s_lshr_b32 s38, s4, 1
	v_and_b32_e32 v26, 31, v167
	v_and_b32_e32 v27, 3, v167
	v_bfe_u32 v28, v167, 3, 1
	v_bfe_u32 v29, v167, 2, 1
	v_lshl_or_b32 v27, v28, 2, v27
	v_lshl_or_b32 v27, v29, 3, v27
	v_lshlrev_b32_e32 v32, 9, v182
	v_lshl_add_u32 v30, v27, 3, v32
	v_add_u32_e32 v30, 0x10000, v30
	v_lshl_add_u32 v31, v26, 3, v32
	v_add_u32_e32 v31, 0x10400, v31
	v_xor_b32_e32 v28, 31, v26
	v_lshl_add_u32 v28, v28, 3, v32
	v_add_u32_e32 v28, 0x10400, v28
	v_bfe_u32 v29, v167, 4, 1
	v_mul_u32_u24_e32 v29, 0x78, v29
	v_xor_b32_e32 v254, s38, v29
	v_or_b32_e32 v254, 0x10800, v254
	v_and_b32_e32 v33, 16, v167
	v_cmp_eq_u32_e32 vcc, 0, v33
	ds_read2_b64 v[66:69], v30 offset0:0 offset1:32
	ds_read2_b64 v[70:73], v30 offset0:16 offset1:48
	ds_read2_b64 v[198:201], v31 offset0:0 offset1:32
	ds_read2_b64 v[202:205], v28 offset0:0 offset1:32
	ds_read2_b64 v[206:209], v254 offset0:0 offset1:16
	ds_read2_b64 v[210:213], v254 offset0:32 offset1:48
	s_waitcnt lgkmcnt(0)
	v_cndmask_b32_e32 v74, v67, v66, vcc
	v_cndmask_b32_e32 v75, v69, v68, vcc
	v_cndmask_b32_e64 v76, v66, -v67, vcc
	v_cndmask_b32_e64 v77, v68, -v69, vcc
	v_cndmask_b32_e32 v78, v71, v70, vcc
	v_cndmask_b32_e32 v79, v73, v72, vcc
	v_cndmask_b32_e64 v80, v70, -v71, vcc
	v_cndmask_b32_e64 v81, v72, -v73, vcc
	v_cvt_pk_f16_f32 v190, v74, v75
	v_cvt_pk_f16_f32 v191, v74, v75
	v_cvt_pk_f16_f32 v192, v76, v77
	v_cvt_pk_f16_f32 v193, v76, v77
	v_cvt_pk_f16_f32 v194, v78, v79
	v_cvt_pk_f16_f32 v195, v78, v79
	v_cvt_pk_f16_f32 v196, v80, v81
	v_cvt_pk_f16_f32 v197, v80, v81
	v_mul_f32_e32 v66, v199, v207
	v_mul_f32_e32 v68, v199, v206
	v_mul_f32_e32 v67, v199, v209
	v_mul_f32_e32 v69, v199, v208
	v_fma_f32 v66, v198, v206, -v66
	v_fma_f32 v68, v198, v207, v68
	v_fma_f32 v67, v198, v208, -v67
	v_fma_f32 v69, v198, v209, v69
	v_cvt_pk_f16_f32 v214, v66, v67
	v_cvt_pk_f16_f32 v216, v68, v69
	v_mul_f32_e32 v70, v201, v211
	v_mul_f32_e32 v72, v201, v210
	v_mul_f32_e32 v71, v201, v213
	v_mul_f32_e32 v73, v201, v212
	v_fma_f32 v70, v200, v210, -v70
	v_fma_f32 v72, v200, v211, v72
	v_fma_f32 v71, v200, v212, -v71
	v_fma_f32 v73, v200, v213, v73
	v_cvt_pk_f16_f32 v215, v70, v71
	v_cvt_pk_f16_f32 v217, v72, v73
	v_mul_f32_e32 v66, v203, v207
	v_mul_f32_e32 v68, v203, v206
	v_mul_f32_e32 v67, v203, v209
	v_mul_f32_e32 v69, v203, v208
	v_fma_f32 v66, v202, v206, -v66
	v_fma_f32 v68, v202, v207, v68
	v_fma_f32 v67, v202, v208, -v67
	v_fma_f32 v69, v202, v209, v69
	v_cvt_pk_f16_f32 v218, v66, v67
	v_cvt_pk_f16_f32 v220, v68, v69
	v_mul_f32_e32 v70, v205, v211
	v_mul_f32_e32 v72, v205, v210
	v_mul_f32_e32 v71, v205, v213
	v_mul_f32_e32 v73, v205, v212
	v_fma_f32 v70, v204, v210, -v70
	v_fma_f32 v72, v204, v211, v72
	v_fma_f32 v71, v204, v212, -v71
	v_fma_f32 v73, v204, v213, v73
	v_cvt_pk_f16_f32 v219, v70, v71
	v_cvt_pk_f16_f32 v221, v72, v73
	v_xor_b32_e32 v255, 8, v254
	ds_read2_b64 v[206:209], v255 offset0:0 offset1:16
	ds_read2_b64 v[210:213], v255 offset0:32 offset1:48
	v_mfma_f32_32x32x16_f16 v[2:17], v[190:193], v[214:217], 0
	v_mfma_f32_32x32x16_f16 v[18:33], v[194:197], v[218:221], 0
	s_waitcnt lgkmcnt(0)
	v_mul_f32_e32 v66, v199, v207
	v_mul_f32_e32 v68, v199, v206
	v_mul_f32_e32 v67, v199, v209
	v_mul_f32_e32 v69, v199, v208
	v_fma_f32 v66, v198, v206, -v66
	v_fma_f32 v68, v198, v207, v68
	v_fma_f32 v67, v198, v208, -v67
	v_fma_f32 v69, v198, v209, v69
	v_cvt_pk_f16_f32 v214, v66, v67
	v_cvt_pk_f16_f32 v216, v68, v69
	v_mul_f32_e32 v70, v201, v211
	v_mul_f32_e32 v72, v201, v210
	v_mul_f32_e32 v71, v201, v213
	v_mul_f32_e32 v73, v201, v212
	v_fma_f32 v70, v200, v210, -v70
	v_fma_f32 v72, v200, v211, v72
	v_fma_f32 v71, v200, v212, -v71
	v_fma_f32 v73, v200, v213, v73
	v_cvt_pk_f16_f32 v215, v70, v71
	v_cvt_pk_f16_f32 v217, v72, v73
	v_cvt_pk_f16_f32 v2, v2, v3
	v_cvt_pk_f16_f32 v3, v4, v5
	v_cvt_pk_f16_f32 v4, v6, v7
	v_cvt_pk_f16_f32 v5, v8, v9
	v_cvt_pk_f16_f32 v6, v10, v11
	v_cvt_pk_f16_f32 v7, v12, v13
	v_cvt_pk_f16_f32 v8, v14, v15
	v_cvt_pk_f16_f32 v9, v16, v17
	v_cvt_pk_f16_f32 v18, v18, v19
	v_cvt_pk_f16_f32 v19, v20, v21
	v_cvt_pk_f16_f32 v20, v22, v23
	v_cvt_pk_f16_f32 v21, v24, v25
	v_cvt_pk_f16_f32 v22, v26, v27
	v_cvt_pk_f16_f32 v23, v28, v29
	v_cvt_pk_f16_f32 v24, v30, v31
	v_cvt_pk_f16_f32 v25, v32, v33
	s_cmp_eq_u32 s35, 0
	s_cbranch_scc1 .Lprio1_old
	s_setprio 2
	s_branch .Lprio1_done
.Lprio1_old:
	s_setprio 1
.Lprio1_done:
	s_waitcnt vmcnt(6)
	v_mul_f32_e32 v66, v203, v207
	v_mul_f32_e32 v68, v203, v206
	v_mfma_f32_32x32x16_f16 v[34:49], v[2:5], v[150:153], 0
	v_mul_f32_e32 v67, v203, v209
	v_mul_f32_e32 v69, v203, v208
	v_mfma_f32_32x32x16_f16 v[34:49], v[18:21], v[146:149], v[34:49]
	v_fma_f32 v66, v202, v206, -v66
	v_fma_f32 v68, v202, v207, v68
	v_mfma_f32_32x32x16_f16 v[34:49], v[6:9], v[142:145], v[34:49]
	v_fma_f32 v67, v202, v208, -v67
	v_fma_f32 v69, v202, v209, v69
	v_mfma_f32_32x32x16_f16 v[34:49], v[22:25], v[138:141], v[34:49]
	v_cvt_pk_f16_f32 v218, v66, v67
	v_cvt_pk_f16_f32 v220, v68, v69
	s_waitcnt vmcnt(2)
	v_mul_f32_e32 v70, v205, v211
	v_mul_f32_e32 v72, v205, v210
	v_mfma_f32_32x32x16_f16 v[50:65], v[2:5], v[134:137], 0
	v_mul_f32_e32 v71, v205, v213
	v_mul_f32_e32 v73, v205, v212
	v_mfma_f32_32x32x16_f16 v[50:65], v[18:21], v[126:129], v[50:65]
	v_fma_f32 v70, v204, v210, -v70
	v_fma_f32 v72, v204, v211, v72
	v_mfma_f32_32x32x16_f16 v[50:65], v[6:9], v[122:125], v[50:65]
	v_fma_f32 v71, v204, v212, -v71
	v_fma_f32 v73, v204, v213, v73
	v_mfma_f32_32x32x16_f16 v[50:65], v[22:25], v[130:133], v[50:65]
	v_cvt_pk_f16_f32 v219, v70, v71
	v_cvt_pk_f16_f32 v221, v72, v73
	v_xor_b32_e32 v255, 16, v254
	ds_read2_b64 v[206:209], v255 offset0:0 offset1:16
	ds_read2_b64 v[210:213], v255 offset0:32 offset1:48
	v_mfma_f32_32x32x16_f16 v[2:17], v[190:193], v[214:217], 0
	v_mfma_f32_32x32x16_f16 v[18:33], v[194:197], v[218:221], 0
	v_cvt_pk_f16_f32 v34, v34, v35
	v_cvt_pk_f16_f32 v35, v36, v37
	v_cvt_pk_f16_f32 v36, v38, v39
	v_cvt_pk_f16_f32 v37, v40, v41
	v_cvt_pk_f16_f32 v38, v42, v43
	v_cvt_pk_f16_f32 v39, v44, v45
	v_cvt_pk_f16_f32 v40, v46, v47
	v_cvt_pk_f16_f32 v41, v48, v49
	v_cvt_pk_f16_f32 v50, v50, v51
	v_cvt_pk_f16_f32 v51, v52, v53
	v_cvt_pk_f16_f32 v52, v54, v55
	v_cvt_pk_f16_f32 v53, v56, v57
	v_cvt_pk_f16_f32 v54, v58, v59
	v_cvt_pk_f16_f32 v55, v60, v61
	v_cvt_pk_f16_f32 v56, v62, v63
	v_cvt_pk_f16_f32 v57, v64, v65
	s_waitcnt vmcnt(2)
	v_cvt_pk_f16_f32 v2, v2, v3
	v_cvt_pk_f16_f32 v3, v4, v5
	v_cvt_pk_f16_f32 v4, v6, v7
	v_cvt_pk_f16_f32 v5, v8, v9
	v_mfma_f32_32x32x16_f16 v[90:105], v[34:37], v[222:225], 0
	v_cvt_pk_f16_f32 v6, v10, v11
	v_cvt_pk_f16_f32 v7, v12, v13
	v_cvt_pk_f16_f32 v8, v14, v15
	v_cvt_pk_f16_f32 v9, v16, v17
	v_mfma_f32_32x32x16_f16 v[106:121], v[34:37], v[238:241], 0
	v_cvt_pk_f16_f32 v18, v18, v19
	v_cvt_pk_f16_f32 v19, v20, v21
	v_cvt_pk_f16_f32 v20, v22, v23
	v_cvt_pk_f16_f32 v21, v24, v25
	v_mfma_f32_32x32x16_f16 v[90:105], v[38:41], v[226:229], v[90:105]
	v_cvt_pk_f16_f32 v22, v26, v27
	v_cvt_pk_f16_f32 v23, v28, v29
	v_cvt_pk_f16_f32 v24, v30, v31
	v_cvt_pk_f16_f32 v25, v32, v33
	v_mfma_f32_32x32x16_f16 v[106:121], v[38:41], v[242:245], v[106:121]
	s_waitcnt lgkmcnt(0)
	v_mul_f32_e32 v66, v199, v207
	v_mul_f32_e32 v68, v199, v206
	v_mul_f32_e32 v67, v199, v209
	v_mfma_f32_32x32x16_f16 v[90:105], v[50:53], v[230:233], v[90:105]
	v_mul_f32_e32 v69, v199, v208
	v_fma_f32 v66, v198, v206, -v66
	v_fma_f32 v68, v198, v207, v68
	v_fma_f32 v67, v198, v208, -v67
	v_mfma_f32_32x32x16_f16 v[106:121], v[50:53], v[246:249], v[106:121]
	v_fma_f32 v69, v198, v209, v69
	v_cvt_pk_f16_f32 v214, v66, v67
	v_cvt_pk_f16_f32 v216, v68, v69
	v_mul_f32_e32 v70, v201, v211
	v_mfma_f32_32x32x16_f16 v[90:105], v[54:57], v[234:237], v[90:105]
	v_mul_f32_e32 v72, v201, v210
	v_mul_f32_e32 v71, v201, v213
	v_mul_f32_e32 v73, v201, v212
	v_fma_f32 v70, v200, v210, -v70
	v_mfma_f32_32x32x16_f16 v[106:121], v[54:57], v[250:253], v[106:121]
	v_fma_f32 v72, v200, v211, v72
	v_fma_f32 v71, v200, v212, -v71
	v_fma_f32 v73, v200, v213, v73
	v_cvt_pk_f16_f32 v215, v70, v71
	v_cvt_pk_f16_f32 v217, v72, v73
	v_mfma_f32_32x32x16_f16 v[34:49], v[2:5], v[150:153], 0
	v_mul_f32_e32 v66, v203, v207
	v_mul_f32_e32 v68, v203, v206
	v_mul_f32_e32 v67, v203, v209
	v_mul_f32_e32 v69, v203, v208
	v_fma_f32 v66, v202, v206, -v66
	v_mfma_f32_32x32x16_f16 v[34:49], v[18:21], v[146:149], v[34:49]
	v_fma_f32 v68, v202, v207, v68
	v_fma_f32 v67, v202, v208, -v67
	v_fma_f32 v69, v202, v209, v69
	v_cvt_pk_f16_f32 v218, v66, v67
	v_cvt_pk_f16_f32 v220, v68, v69
	v_mfma_f32_32x32x16_f16 v[34:49], v[6:9], v[142:145], v[34:49]
	v_mul_f32_e32 v70, v205, v211
	v_mul_f32_e32 v72, v205, v210
	v_mul_f32_e32 v71, v205, v213
	v_mul_f32_e32 v73, v205, v212
	v_fma_f32 v70, v204, v210, -v70
	v_mfma_f32_32x32x16_f16 v[34:49], v[22:25], v[138:141], v[34:49]
	v_fma_f32 v72, v204, v211, v72
	v_fma_f32 v71, v204, v212, -v71
	v_fma_f32 v73, v204, v213, v73
	v_cvt_pk_f16_f32 v219, v70, v71
	v_cvt_pk_f16_f32 v221, v72, v73
	v_mfma_f32_32x32x16_f16 v[50:65], v[2:5], v[134:137], 0
	v_cvt_pk_f16_f32 v90, v90, v91
	v_cvt_pk_f16_f32 v91, v92, v93
	v_cvt_pk_f16_f32 v92, v94, v95
	v_cvt_pk_f16_f32 v93, v96, v97
	v_cvt_pk_f16_f32 v94, v98, v99
	v_mfma_f32_32x32x16_f16 v[50:65], v[18:21], v[126:129], v[50:65]
	v_cvt_pk_f16_f32 v95, v100, v101
	v_cvt_pk_f16_f32 v96, v102, v103
	v_cvt_pk_f16_f32 v97, v104, v105
	v_cvt_pk_f16_f32 v106, v106, v107
	v_cvt_pk_f16_f32 v107, v108, v109
	v_mfma_f32_32x32x16_f16 v[50:65], v[6:9], v[122:125], v[50:65]
	v_cvt_pk_f16_f32 v108, v110, v111
	v_cvt_pk_f16_f32 v109, v112, v113
	v_cvt_pk_f16_f32 v110, v114, v115
	v_cvt_pk_f16_f32 v111, v116, v117
	v_cvt_pk_f16_f32 v112, v118, v119
	v_mfma_f32_32x32x16_f16 v[50:65], v[22:25], v[130:133], v[50:65]
	v_cvt_pk_f16_f32 v113, v120, v121
	ds_write_b128 v173, v[90:93]
	ds_write_b128 v172, v[94:97]
	ds_write_b128 v173, v[106:109] offset:32768
	ds_write_b128 v172, v[110:113] offset:32768
	v_xor_b32_e32 v255, 24, v254
	ds_read2_b64 v[206:209], v255 offset0:0 offset1:16
	ds_read2_b64 v[210:213], v255 offset0:32 offset1:48
	v_mfma_f32_32x32x16_f16 v[2:17], v[190:193], v[214:217], 0
	v_mfma_f32_32x32x16_f16 v[18:33], v[194:197], v[218:221], 0
	v_cvt_pk_f16_f32 v34, v34, v35
	v_cvt_pk_f16_f32 v35, v36, v37
	v_cvt_pk_f16_f32 v36, v38, v39
	v_cvt_pk_f16_f32 v37, v40, v41
	v_cvt_pk_f16_f32 v38, v42, v43
	v_cvt_pk_f16_f32 v39, v44, v45
	v_cvt_pk_f16_f32 v40, v46, v47
	v_cvt_pk_f16_f32 v41, v48, v49
	v_cvt_pk_f16_f32 v50, v50, v51
	v_cvt_pk_f16_f32 v51, v52, v53
	v_cvt_pk_f16_f32 v52, v54, v55
	v_cvt_pk_f16_f32 v53, v56, v57
	v_cvt_pk_f16_f32 v54, v58, v59
	v_cvt_pk_f16_f32 v55, v60, v61
	v_cvt_pk_f16_f32 v56, v62, v63
	v_cvt_pk_f16_f32 v57, v64, v65
	v_mfma_f32_32x32x16_f16 v[90:105], v[34:37], v[222:225], 0
	v_cvt_pk_f16_f32 v2, v2, v3
	v_cvt_pk_f16_f32 v3, v4, v5
	v_cvt_pk_f16_f32 v4, v6, v7
	v_cvt_pk_f16_f32 v5, v8, v9
	v_mfma_f32_32x32x16_f16 v[106:121], v[34:37], v[238:241], 0
	v_cvt_pk_f16_f32 v6, v10, v11
	v_cvt_pk_f16_f32 v7, v12, v13
	v_cvt_pk_f16_f32 v8, v14, v15
	v_cvt_pk_f16_f32 v9, v16, v17
	v_cvt_pk_f16_f32 v18, v18, v19
	v_mfma_f32_32x32x16_f16 v[90:105], v[38:41], v[226:229], v[90:105]
	v_cvt_pk_f16_f32 v19, v20, v21
	v_cvt_pk_f16_f32 v20, v22, v23
	v_cvt_pk_f16_f32 v21, v24, v25
	v_cvt_pk_f16_f32 v22, v26, v27
	v_mfma_f32_32x32x16_f16 v[106:121], v[38:41], v[242:245], v[106:121]
	v_cvt_pk_f16_f32 v23, v28, v29
	v_cvt_pk_f16_f32 v24, v30, v31
	v_cvt_pk_f16_f32 v25, v32, v33
	s_waitcnt lgkmcnt(0)
	v_mul_f32_e32 v66, v199, v207
	v_mfma_f32_32x32x16_f16 v[90:105], v[50:53], v[230:233], v[90:105]
	v_mul_f32_e32 v68, v199, v206
	v_mul_f32_e32 v67, v199, v209
	v_mul_f32_e32 v69, v199, v208
	v_fma_f32 v66, v198, v206, -v66
	v_fma_f32 v68, v198, v207, v68
	v_mfma_f32_32x32x16_f16 v[106:121], v[50:53], v[246:249], v[106:121]
	v_fma_f32 v67, v198, v208, -v67
	v_fma_f32 v69, v198, v209, v69
	v_cvt_pk_f16_f32 v214, v66, v67
	v_cvt_pk_f16_f32 v216, v68, v69
	v_mfma_f32_32x32x16_f16 v[90:105], v[54:57], v[234:237], v[90:105]
	v_mul_f32_e32 v70, v201, v211
	v_mul_f32_e32 v72, v201, v210
	v_mul_f32_e32 v71, v201, v213
	v_mul_f32_e32 v73, v201, v212
	v_fma_f32 v70, v200, v210, -v70
	v_mfma_f32_32x32x16_f16 v[106:121], v[54:57], v[250:253], v[106:121]
	v_fma_f32 v72, v200, v211, v72
	v_fma_f32 v71, v200, v212, -v71
	v_fma_f32 v73, v200, v213, v73
	v_cvt_pk_f16_f32 v215, v70, v71
	v_cvt_pk_f16_f32 v217, v72, v73
	v_mfma_f32_32x32x16_f16 v[34:49], v[2:5], v[150:153], 0
	v_mul_f32_e32 v66, v203, v207
	v_mul_f32_e32 v68, v203, v206
	v_mul_f32_e32 v67, v203, v209
	v_mul_f32_e32 v69, v203, v208
	v_fma_f32 v66, v202, v206, -v66
	v_mfma_f32_32x32x16_f16 v[34:49], v[18:21], v[146:149], v[34:49]
	v_fma_f32 v68, v202, v207, v68
	v_fma_f32 v67, v202, v208, -v67
	v_fma_f32 v69, v202, v209, v69
	v_cvt_pk_f16_f32 v218, v66, v67
	v_cvt_pk_f16_f32 v220, v68, v69
	v_mfma_f32_32x32x16_f16 v[34:49], v[6:9], v[142:145], v[34:49]
	v_mul_f32_e32 v70, v205, v211
	v_mul_f32_e32 v72, v205, v210
	v_mul_f32_e32 v71, v205, v213
	v_mul_f32_e32 v73, v205, v212
	v_fma_f32 v70, v204, v210, -v70
	v_mfma_f32_32x32x16_f16 v[34:49], v[22:25], v[138:141], v[34:49]
	v_fma_f32 v72, v204, v211, v72
	v_fma_f32 v71, v204, v212, -v71
	v_fma_f32 v73, v204, v213, v73
	v_cvt_pk_f16_f32 v219, v70, v71
	v_cvt_pk_f16_f32 v221, v72, v73
	v_cvt_pk_f16_f32 v90, v90, v91
	v_mfma_f32_32x32x16_f16 v[50:65], v[2:5], v[134:137], 0
	v_cvt_pk_f16_f32 v91, v92, v93
	v_cvt_pk_f16_f32 v92, v94, v95
	v_cvt_pk_f16_f32 v93, v96, v97
	v_cvt_pk_f16_f32 v94, v98, v99
	v_cvt_pk_f16_f32 v95, v100, v101
	v_mfma_f32_32x32x16_f16 v[50:65], v[18:21], v[126:129], v[50:65]
	v_cvt_pk_f16_f32 v96, v102, v103
	v_cvt_pk_f16_f32 v97, v104, v105
	v_cvt_pk_f16_f32 v106, v106, v107
	v_cvt_pk_f16_f32 v107, v108, v109
	v_cvt_pk_f16_f32 v108, v110, v111
	v_mfma_f32_32x32x16_f16 v[50:65], v[6:9], v[122:125], v[50:65]
	v_cvt_pk_f16_f32 v109, v112, v113
	v_cvt_pk_f16_f32 v110, v114, v115
	v_cvt_pk_f16_f32 v111, v116, v117
	v_cvt_pk_f16_f32 v112, v118, v119
	v_cvt_pk_f16_f32 v113, v120, v121
	v_mfma_f32_32x32x16_f16 v[50:65], v[22:25], v[130:133], v[50:65]
	v_xor_b32_e32 v74, 0x8a0, v173
	v_xor_b32_e32 v75, 0x8a0, v172
	ds_write_b128 v74, v[90:93]
	ds_write_b128 v75, v[94:97]
	ds_write_b128 v74, v[106:109] offset:32768
	ds_write_b128 v75, v[110:113] offset:32768
	s_nop 0
	v_mfma_f32_32x32x16_f16 v[2:17], v[190:193], v[214:217], 0
	v_mfma_f32_32x32x16_f16 v[18:33], v[194:197], v[218:221], 0
	v_cvt_pk_f16_f32 v34, v34, v35
	v_cvt_pk_f16_f32 v35, v36, v37
	v_cvt_pk_f16_f32 v36, v38, v39
	v_cvt_pk_f16_f32 v37, v40, v41
	v_cvt_pk_f16_f32 v38, v42, v43
	v_cvt_pk_f16_f32 v39, v44, v45
	v_cvt_pk_f16_f32 v40, v46, v47
	v_cvt_pk_f16_f32 v41, v48, v49
	v_cvt_pk_f16_f32 v50, v50, v51
	v_cvt_pk_f16_f32 v51, v52, v53
	v_cvt_pk_f16_f32 v52, v54, v55
	v_cvt_pk_f16_f32 v53, v56, v57
	v_cvt_pk_f16_f32 v54, v58, v59
	v_cvt_pk_f16_f32 v55, v60, v61
	v_cvt_pk_f16_f32 v56, v62, v63
	v_cvt_pk_f16_f32 v57, v64, v65
	v_mfma_f32_32x32x16_f16 v[90:105], v[34:37], v[222:225], 0
	v_cvt_pk_f16_f32 v2, v2, v3
	v_cvt_pk_f16_f32 v3, v4, v5
	v_mfma_f32_32x32x16_f16 v[106:121], v[34:37], v[238:241], 0
	v_cvt_pk_f16_f32 v4, v6, v7
	v_cvt_pk_f16_f32 v5, v8, v9
	v_mfma_f32_32x32x16_f16 v[90:105], v[38:41], v[226:229], v[90:105]
	v_cvt_pk_f16_f32 v6, v10, v11
	v_cvt_pk_f16_f32 v7, v12, v13
	v_mfma_f32_32x32x16_f16 v[106:121], v[38:41], v[242:245], v[106:121]
	v_cvt_pk_f16_f32 v8, v14, v15
	v_cvt_pk_f16_f32 v9, v16, v17
	v_mfma_f32_32x32x16_f16 v[90:105], v[50:53], v[230:233], v[90:105]
	v_cvt_pk_f16_f32 v18, v18, v19
	v_cvt_pk_f16_f32 v19, v20, v21
	v_mfma_f32_32x32x16_f16 v[106:121], v[50:53], v[246:249], v[106:121]
	v_cvt_pk_f16_f32 v20, v22, v23
	v_cvt_pk_f16_f32 v21, v24, v25
	v_mfma_f32_32x32x16_f16 v[90:105], v[54:57], v[234:237], v[90:105]
	v_cvt_pk_f16_f32 v22, v26, v27
	v_cvt_pk_f16_f32 v23, v28, v29
	v_mfma_f32_32x32x16_f16 v[106:121], v[54:57], v[250:253], v[106:121]
	v_cvt_pk_f16_f32 v24, v30, v31
	v_cvt_pk_f16_f32 v25, v32, v33
	v_mfma_f32_32x32x16_f16 v[34:49], v[2:5], v[150:153], 0
	v_mfma_f32_32x32x16_f16 v[34:49], v[18:21], v[146:149], v[34:49]
	v_mfma_f32_32x32x16_f16 v[34:49], v[6:9], v[142:145], v[34:49]
	v_mfma_f32_32x32x16_f16 v[34:49], v[22:25], v[138:141], v[34:49]
	v_mfma_f32_32x32x16_f16 v[50:65], v[2:5], v[134:137], 0
	s_nop 5
	v_cvt_pk_f16_f32 v90, v90, v91
	v_cvt_pk_f16_f32 v91, v92, v93
	v_cvt_pk_f16_f32 v92, v94, v95
	v_cvt_pk_f16_f32 v93, v96, v97
	v_mfma_f32_32x32x16_f16 v[50:65], v[18:21], v[126:129], v[50:65]
	v_cvt_pk_f16_f32 v94, v98, v99
	v_cvt_pk_f16_f32 v95, v100, v101
	v_cvt_pk_f16_f32 v96, v102, v103
	v_cvt_pk_f16_f32 v97, v104, v105
	v_cvt_pk_f16_f32 v106, v106, v107
	v_cvt_pk_f16_f32 v107, v108, v109
	v_mfma_f32_32x32x16_f16 v[50:65], v[6:9], v[122:125], v[50:65]
	v_cvt_pk_f16_f32 v108, v110, v111
	v_cvt_pk_f16_f32 v109, v112, v113
	v_cvt_pk_f16_f32 v110, v114, v115
	v_cvt_pk_f16_f32 v111, v116, v117
	v_cvt_pk_f16_f32 v112, v118, v119
	v_cvt_pk_f16_f32 v113, v120, v121
	v_mfma_f32_32x32x16_f16 v[50:65], v[22:25], v[130:133], v[50:65]
	v_xor_b32_e32 v74, 0x1040, v173
	v_xor_b32_e32 v75, 0x1040, v172
	ds_write_b128 v74, v[90:93]
	ds_write_b128 v75, v[94:97]
	ds_write_b128 v74, v[106:109] offset:32768
	ds_write_b128 v75, v[110:113] offset:32768
	s_nop 11
	v_cvt_pk_f16_f32 v34, v34, v35
	v_cvt_pk_f16_f32 v35, v36, v37
	v_cvt_pk_f16_f32 v36, v38, v39
	v_cvt_pk_f16_f32 v37, v40, v41
	v_cvt_pk_f16_f32 v38, v42, v43
	v_cvt_pk_f16_f32 v39, v44, v45
	v_cvt_pk_f16_f32 v40, v46, v47
	v_cvt_pk_f16_f32 v41, v48, v49
	v_cvt_pk_f16_f32 v50, v50, v51
	v_cvt_pk_f16_f32 v51, v52, v53
	v_cvt_pk_f16_f32 v52, v54, v55
	v_cvt_pk_f16_f32 v53, v56, v57
	v_cvt_pk_f16_f32 v54, v58, v59
	v_cvt_pk_f16_f32 v55, v60, v61
	v_cvt_pk_f16_f32 v56, v62, v63
	v_cvt_pk_f16_f32 v57, v64, v65
	v_mfma_f32_32x32x16_f16 v[90:105], v[34:37], v[222:225], 0
	v_mfma_f32_32x32x16_f16 v[106:121], v[34:37], v[238:241], 0
	v_mfma_f32_32x32x16_f16 v[90:105], v[38:41], v[226:229], v[90:105]
	v_mfma_f32_32x32x16_f16 v[106:121], v[38:41], v[242:245], v[106:121]
	v_mfma_f32_32x32x16_f16 v[90:105], v[50:53], v[230:233], v[90:105]
	v_mfma_f32_32x32x16_f16 v[106:121], v[50:53], v[246:249], v[106:121]
	v_mfma_f32_32x32x16_f16 v[90:105], v[54:57], v[234:237], v[90:105]
	v_mfma_f32_32x32x16_f16 v[106:121], v[54:57], v[250:253], v[106:121]
	v_and_b32_e32 v134, 1, v156
	v_bitop3_b32 v132, v171, s40, v170 bitop3:0x36
	v_bitop3_b32 v131, s41, v154, v160 bitop3:0x36
	v_bitop3_b32 v135, v171, s42, v170 bitop3:0x36
	v_xor_b32_e32 v133, s43, v154
	v_and_b32_e32 v130, 4, v156
	s_lshl_b32 s2, s27, 3
	s_lshl_b32 s3, s5, 2
	s_or_b32 s2, s3, s2
	s_ashr_i32 s3, s2, 31
	s_lshl_b64 s[2:3], s[2:3], 13
	s_add_u32 s2, s20, s2
	s_addc_u32 s3, s21, s3
	v_lshlrev_b32_e32 v154, 1, v169
	v_lshl_add_u64 v[2:3], s[2:3], 0, v[154:155]
	v_add_co_u32_e32 v2, vcc, s23, v2
	s_nop 1
	v_addc_co_u32_e32 v3, vcc, 0, v3, vcc
	v_cvt_pk_f16_f32 v90, v90, v91
	v_cvt_pk_f16_f32 v91, v92, v93
	v_cvt_pk_f16_f32 v92, v94, v95
	v_cvt_pk_f16_f32 v93, v96, v97
	v_cvt_pk_f16_f32 v94, v98, v99
	v_cvt_pk_f16_f32 v95, v100, v101
	v_cvt_pk_f16_f32 v96, v102, v103
	v_cvt_pk_f16_f32 v97, v104, v105
	v_cvt_pk_f16_f32 v106, v106, v107
	v_cvt_pk_f16_f32 v107, v108, v109
	v_cvt_pk_f16_f32 v108, v110, v111
	v_cvt_pk_f16_f32 v109, v112, v113
	v_cvt_pk_f16_f32 v110, v114, v115
	v_cvt_pk_f16_f32 v111, v116, v117
	v_cvt_pk_f16_f32 v112, v118, v119
	v_cvt_pk_f16_f32 v113, v120, v121
	v_xor_b32_e32 v74, 0x18e0, v173
	v_xor_b32_e32 v75, 0x18e0, v172
	ds_write_b128 v74, v[90:93]
	ds_write_b128 v75, v[94:97]
	ds_write_b128 v74, v[106:109] offset:32768
	ds_write_b128 v75, v[110:113] offset:32768
	s_cmp_eq_u32 s35, 0
	s_cbranch_scc1 .Lprio2_old
	s_setprio 1
	s_branch .Lprio2_done
.Lprio2_old:
	s_setprio 0
.Lprio2_done:
	s_waitcnt lgkmcnt(0)
	s_barrier
	global_load_dwordx4 v[62:65], v154, s[2:3]
	global_load_dwordx4 v[46:49], v154, s[2:3] offset:1024
	global_load_dwordx4 v[42:45], v154, s[2:3] offset:2048
	global_load_dwordx4 v[38:41], v154, s[2:3] offset:3072
	global_load_dwordx4 v[54:57], v[2:3], off offset:1024
	global_load_dwordx4 v[50:53], v[2:3], off offset:2048
	v_lshl_add_u64 v[4:5], s[12:13], 0, v[154:155]
	global_load_dwordx4 v[126:129], v154, s[12:13]
	global_load_dwordx4 v[122:125], v154, s[12:13] offset:1024
	global_load_dwordx4 v[118:121], v154, s[12:13] offset:2048
	global_load_dwordx4 v[114:117], v154, s[12:13] offset:3072
	global_load_dwordx4 v[34:37], v168, s[2:3]
	global_load_dwordx4 v[110:113], v168, s[12:13]
	v_add_co_u32_e32 v4, vcc, s23, v4
	s_nop 1
	v_addc_co_u32_e32 v5, vcc, 0, v5, vcc
	global_load_dwordx4 v[58:61], v[2:3], off offset:3072
	global_load_dwordx4 v[106:109], v[4:5], off offset:1024
	global_load_dwordx4 v[94:97], v[4:5], off offset:2048
	global_load_dwordx4 v[90:93], v[4:5], off offset:3072
	v_bfrev_b32_e32 v3, v156
	v_lshlrev_b32_e32 v7, 5, v167
	v_lshlrev_b32_e32 v6, 9, v167
	v_and_b32_e32 v7, 0x200, v7
	v_lshlrev_b32_e32 v8, 8, v167
	v_lshrrev_b32_e32 v3, 27, v3
	v_lshrrev_b32_e32 v2, 2, v167
	v_lshrrev_b32_e32 v4, 4, v156
	v_xor_b32_e32 v5, v169, v156
	v_and_b32_e32 v6, 0x5800, v6
	v_and_b32_e32 v3, 8, v3
	v_and_or_b32 v7, v8, s24, v7
	v_lshrrev_b32_e32 v5, 1, v5
	v_xor_b32_e32 v4, v2, v4
	v_or3_b32 v3, v7, v6, v3
	v_bitop3_b32 v7, v2, v182, 1 bitop3:0x6c
	v_lshlrev_b32_e32 v2, 1, v167
	v_and_b32_e32 v5, 4, v5
	v_lshlrev_b32_e32 v4, 3, v4
	v_lshrrev_b32_e32 v6, 1, v167
	v_and_b32_e32 v2, 2, v2
	v_and_or_b32 v9, v169, 8, v2
	v_and_b32_e32 v2, 8, v4
	v_and_or_b32 v4, v6, 2, v5
	v_or3_b32 v2, v4, v2, v134
	v_lshlrev_b32_e32 v2, 4, v2
	v_bitop3_b32 v146, v3, s28, v2 bitop3:0x36
	v_xor_b32_e32 v8, v6, v182
	v_xor_b32_e32 v147, 0x2010, v146
	v_lshlrev_b32_e32 v8, 2, v8
	v_and_b32_e32 v8, 4, v8
	v_or3_b32 v6, v9, v7, v8
	v_lshlrev_b32_e32 v7, 11, v167
	v_and_b32_e32 v8, 0x7800, v7
	v_lshlrev_b32_e32 v6, 4, v6
	v_or3_b32 v22, v6, v8, v170
	v_and_b32_e32 v23, 0x8000, v7
	v_xor_b32_e32 v150, 16, v146
	v_xad_u32 v70, v22, s28, v23
	v_xor_b32_e32 v151, 0x2000, v146
	ds_read_b64_tr_b16 v[18:19], v146
	ds_read_b64_tr_b16 v[20:21], v147
	ds_read_b64_tr_b16 v[22:23], v146 offset:32768
	ds_read_b64_tr_b16 v[24:25], v147 offset:32768
	ds_read_b64_tr_b16 v[26:27], v150
	ds_read_b64_tr_b16 v[28:29], v151
	ds_read_b64_tr_b16 v[30:31], v150 offset:32768
	ds_read_b64_tr_b16 v[32:33], v151 offset:32768
	v_xor_b32_e32 v148, 32, v146
	v_xor_b32_e32 v149, 0x2030, v146
	v_xor_b32_e32 v144, 48, v146
	v_xor_b32_e32 v145, 0x2020, v146
	v_xor_b32_e32 v142, 64, v146
	v_xor_b32_e32 v143, 0x2050, v146
	v_xor_b32_e32 v140, 0x50, v146
	v_xor_b32_e32 v141, 0x2040, v146
	v_xor_b32_e32 v138, 0x60, v146
	v_xor_b32_e32 v139, 0x2070, v146
	v_xor_b32_e32 v136, 0x70, v146
	v_xor_b32_e32 v137, 0x2060, v146
	v_xor_b32_e32 v71, 0x60, v70
	s_lshl_b64 s[0:1], s[0:1], 13
	s_add_u32 s0, s8, s0
	s_addc_u32 s1, s9, s1
	s_waitcnt vmcnt(17) lgkmcnt(4)
	v_mfma_f32_32x32x16_f16 v[2:17], v[18:21], v[86:89], 0
	s_waitcnt vmcnt(16)
	v_mfma_f32_32x32x16_f16 v[2:17], v[22:25], v[82:85], v[2:17]
	ds_read_b64_tr_b16 v[206:207], v148
	ds_read_b64_tr_b16 v[208:209], v149
	ds_read_b64_tr_b16 v[210:211], v148 offset:32768
	ds_read_b64_tr_b16 v[212:213], v149 offset:32768
	s_waitcnt lgkmcnt(4)
	v_mfma_f32_32x32x16_f16 v[190:205], v[26:29], v[86:89], 0
	v_mfma_f32_32x32x16_f16 v[190:205], v[30:33], v[82:85], v[190:205]
	s_nop 4
	v_cvt_pk_f16_f32 v2, v2, v3
	v_cvt_pk_f16_f32 v3, v4, v5
	v_cvt_pk_f16_f32 v4, v6, v7
	v_cvt_pk_f16_f32 v5, v8, v9
	v_cvt_pk_f16_f32 v6, v10, v11
	v_cvt_pk_f16_f32 v7, v12, v13
	v_cvt_pk_f16_f32 v8, v14, v15
	v_cvt_pk_f16_f32 v9, v16, v17
	v_xor_b32_e32 v73, 0x280, v70
	ds_write_b128 v70, v[2:5]
	ds_write_b128 v73, v[6:9]
	ds_read_b64_tr_b16 v[18:19], v144
	ds_read_b64_tr_b16 v[20:21], v145
	ds_read_b64_tr_b16 v[22:23], v144 offset:32768
	ds_read_b64_tr_b16 v[24:25], v145 offset:32768
	s_waitcnt lgkmcnt(6)
	v_mfma_f32_32x32x16_f16 v[2:17], v[206:209], v[86:89], 0
	v_mfma_f32_32x32x16_f16 v[2:17], v[210:213], v[82:85], v[2:17]
	v_cvt_pk_f16_f32 v190, v190, v191
	v_cvt_pk_f16_f32 v191, v192, v193
	v_cvt_pk_f16_f32 v192, v194, v195
	v_cvt_pk_f16_f32 v193, v196, v197
	v_cvt_pk_f16_f32 v194, v198, v199
	v_cvt_pk_f16_f32 v195, v200, v201
	v_cvt_pk_f16_f32 v196, v202, v203
	v_cvt_pk_f16_f32 v197, v204, v205
	v_xor_b32_e32 v72, 16, v70
	v_xor_b32_e32 v73, 0x290, v70
	ds_write_b128 v72, v[190:193]
	ds_write_b128 v73, v[194:197]
	ds_read_b64_tr_b16 v[26:27], v142
	ds_read_b64_tr_b16 v[28:29], v143
	ds_read_b64_tr_b16 v[30:31], v142 offset:32768
	ds_read_b64_tr_b16 v[32:33], v143 offset:32768
	s_waitcnt lgkmcnt(6)
	v_mfma_f32_32x32x16_f16 v[190:205], v[18:21], v[86:89], 0
	v_mfma_f32_32x32x16_f16 v[190:205], v[22:25], v[82:85], v[190:205]
	v_cvt_pk_f16_f32 v2, v2, v3
	v_cvt_pk_f16_f32 v3, v4, v5
	v_cvt_pk_f16_f32 v4, v6, v7
	v_cvt_pk_f16_f32 v5, v8, v9
	v_cvt_pk_f16_f32 v6, v10, v11
	v_cvt_pk_f16_f32 v7, v12, v13
	v_cvt_pk_f16_f32 v8, v14, v15
	v_cvt_pk_f16_f32 v9, v16, v17
	v_xor_b32_e32 v72, 32, v70
	v_xor_b32_e32 v73, 0x2a0, v70
	ds_write_b128 v72, v[2:5]
	ds_write_b128 v73, v[6:9]
	ds_read_b64_tr_b16 v[206:207], v140
	ds_read_b64_tr_b16 v[208:209], v141
	ds_read_b64_tr_b16 v[210:211], v140 offset:32768
	ds_read_b64_tr_b16 v[212:213], v141 offset:32768
	s_waitcnt lgkmcnt(6)
	v_mfma_f32_32x32x16_f16 v[2:17], v[26:29], v[86:89], 0
	v_mfma_f32_32x32x16_f16 v[2:17], v[30:33], v[82:85], v[2:17]
	v_cvt_pk_f16_f32 v190, v190, v191
	v_cvt_pk_f16_f32 v191, v192, v193
	v_cvt_pk_f16_f32 v192, v194, v195
	v_cvt_pk_f16_f32 v193, v196, v197
	v_cvt_pk_f16_f32 v194, v198, v199
	v_cvt_pk_f16_f32 v195, v200, v201
	v_cvt_pk_f16_f32 v196, v202, v203
	v_cvt_pk_f16_f32 v197, v204, v205
	v_xor_b32_e32 v72, 48, v70
	v_xor_b32_e32 v73, 0x2b0, v70
	ds_write_b128 v72, v[190:193]
	ds_write_b128 v73, v[194:197]
	ds_read_b64_tr_b16 v[18:19], v138
	ds_read_b64_tr_b16 v[20:21], v139
	ds_read_b64_tr_b16 v[22:23], v138 offset:32768
	ds_read_b64_tr_b16 v[24:25], v139 offset:32768
	s_waitcnt lgkmcnt(6)
	v_mfma_f32_32x32x16_f16 v[190:205], v[206:209], v[86:89], 0
	v_mfma_f32_32x32x16_f16 v[190:205], v[210:213], v[82:85], v[190:205]
	v_cvt_pk_f16_f32 v2, v2, v3
	v_cvt_pk_f16_f32 v3, v4, v5
	v_cvt_pk_f16_f32 v4, v6, v7
	v_cvt_pk_f16_f32 v5, v8, v9
	v_cvt_pk_f16_f32 v6, v10, v11
	v_cvt_pk_f16_f32 v7, v12, v13
	v_cvt_pk_f16_f32 v8, v14, v15
	v_cvt_pk_f16_f32 v9, v16, v17
	v_xor_b32_e32 v72, 64, v70
	v_xor_b32_e32 v73, 0x2c0, v70
	ds_write_b128 v72, v[2:5]
	ds_write_b128 v73, v[6:9]
	ds_read_b64_tr_b16 v[26:27], v136
	ds_read_b64_tr_b16 v[28:29], v137
	ds_read_b64_tr_b16 v[30:31], v136 offset:32768
	ds_read_b64_tr_b16 v[32:33], v137 offset:32768
	s_waitcnt lgkmcnt(6)
	v_mfma_f32_32x32x16_f16 v[2:17], v[18:21], v[86:89], 0
	v_mfma_f32_32x32x16_f16 v[2:17], v[22:25], v[82:85], v[2:17]
	v_cvt_pk_f16_f32 v190, v190, v191
	v_cvt_pk_f16_f32 v191, v192, v193
	v_cvt_pk_f16_f32 v192, v194, v195
	v_cvt_pk_f16_f32 v193, v196, v197
	v_cvt_pk_f16_f32 v194, v198, v199
	v_cvt_pk_f16_f32 v195, v200, v201
	v_cvt_pk_f16_f32 v196, v202, v203
	v_cvt_pk_f16_f32 v197, v204, v205
	v_xor_b32_e32 v72, 0x50, v70
	v_xor_b32_e32 v73, 0x2d0, v70
	ds_write_b128 v72, v[190:193]
	ds_write_b128 v73, v[194:197]
	s_waitcnt lgkmcnt(2)
	v_mfma_f32_32x32x16_f16 v[190:205], v[26:29], v[86:89], 0
	v_mfma_f32_32x32x16_f16 v[190:205], v[30:33], v[82:85], v[190:205]
	v_cvt_pk_f16_f32 v2, v2, v3
	v_cvt_pk_f16_f32 v3, v4, v5
	v_cvt_pk_f16_f32 v4, v6, v7
	v_cvt_pk_f16_f32 v5, v8, v9
	v_cvt_pk_f16_f32 v6, v10, v11
	v_cvt_pk_f16_f32 v7, v12, v13
	v_cvt_pk_f16_f32 v8, v14, v15
	v_cvt_pk_f16_f32 v9, v16, v17
	v_xor_b32_e32 v72, 0x60, v70
	v_xor_b32_e32 v73, 0x2e0, v70
	ds_write_b128 v72, v[2:5]
	ds_write_b128 v73, v[6:9]
	v_cvt_pk_f16_f32 v190, v190, v191
	v_cvt_pk_f16_f32 v191, v192, v193
	v_cvt_pk_f16_f32 v192, v194, v195
	v_cvt_pk_f16_f32 v193, v196, v197
	v_cvt_pk_f16_f32 v194, v198, v199
	v_cvt_pk_f16_f32 v195, v200, v201
	v_cvt_pk_f16_f32 v196, v202, v203
	v_cvt_pk_f16_f32 v197, v204, v205
	v_xor_b32_e32 v72, 0x70, v70
	v_xor_b32_e32 v73, 0x2f0, v70
	ds_write_b128 v72, v[190:193]
	ds_write_b128 v73, v[194:197]
	v_lshl_add_u64 v[2:3], s[0:1], 0, v[154:155]
	v_lshl_add_u64 v[4:5], v[2:3], 0, s[18:19]
	v_add_co_u32_e32 v2, vcc, s25, v2
	s_waitcnt lgkmcnt(0)
	s_nop 0
	v_addc_co_u32_e32 v3, vcc, 0, v3, vcc
	s_barrier
	s_nop 0
	s_nop 0
	global_load_dwordx4 v[102:105], v[2:3], off
	global_load_dwordx4 v[98:101], v[4:5], off offset:1024
	s_cmp_eq_u32 s35, 0
	s_cbranch_scc1 .Lprio3_old
	s_setprio 2
	s_branch .Lprio3_done

.Lprio3_done:
	s_add_u32 s0, s2, 0x2000
	s_addc_u32 s1, s3, 0
	v_lshl_add_u64 v[2:3], s[0:1], 0, v[154:155]
	v_add_co_u32_e32 v2, vcc, s23, v2
	global_load_dwordx4 v[66:69], v154, s[0:1]
	global_load_dwordx4 v[70:73], v154, s[0:1] offset:1024
	global_load_dwordx4 v[74:77], v154, s[0:1] offset:2048
	global_load_dwordx4 v[78:81], v154, s[0:1] offset:3072
	v_addc_co_u32_e32 v3, vcc, 0, v3, vcc
	global_load_dwordx4 v[82:85], v168, s[0:1]
	global_load_dwordx4 v[86:89], v[2:3], off offset:1024
	global_load_dwordx4 v[182:185], v[2:3], off offset:2048
	global_load_dwordx4 v[186:189], v[2:3], off offset:3072
	ds_read_b128 v[18:21], v179
	ds_read_b128 v[22:25], v179 offset:32768
	ds_read_b128 v[26:29], v178
	ds_read_b128 v[30:33], v178 offset:32768
	s_add_u32 s0, s2, 0x6000
	s_addc_u32 s1, s3, 0
	s_waitcnt vmcnt(25) lgkmcnt(3)
	v_mfma_f32_32x32x16_f16 v[2:17], v[18:21], v[62:65], 0
	s_add_u32 s2, s2, 0x4000
	s_addc_u32 s3, s3, 0
	s_or_b32 s27, s26, 0x8a0
	s_or_b32 s26, s26, 0xa20
	s_waitcnt vmcnt(24) lgkmcnt(1)
	v_mfma_f32_32x32x16_f16 v[2:17], v[26:29], v[46:49], v[2:17]
	s_waitcnt vmcnt(23)
	v_mfma_f32_32x32x16_f16 v[2:17], v[22:25], v[42:45], v[2:17]
	s_waitcnt vmcnt(22) lgkmcnt(0)
	v_mfma_f32_32x32x16_f16 v[2:17], v[30:33], v[38:41], v[2:17]
	s_waitcnt vmcnt(15)
	v_mfma_f32_32x32x16_f16 v[34:49], v[18:21], v[34:37], 0
	s_nop 9
	v_cvt_pk_f16_f32 v9, v8, v9
	v_cvt_pk_f16_f32 v8, v6, v7
	v_cvt_pk_f16_f32 v7, v4, v5
	v_cvt_pk_f16_f32 v6, v2, v3
	v_cvt_pk_f16_f32 v5, v16, v17
	v_cvt_pk_f16_f32 v4, v14, v15
	v_cvt_pk_f16_f32 v3, v12, v13
	v_mfma_f32_32x32x16_f16 v[34:49], v[26:29], v[54:57], v[34:49]
	v_cvt_pk_f16_f32 v2, v10, v11
	v_mfma_f32_32x32x16_f16 v[34:49], v[22:25], v[50:53], v[34:49]
	s_waitcnt vmcnt(13)
	v_mfma_f32_32x32x16_f16 v[34:49], v[30:33], v[58:61], v[34:49]
	v_mfma_f32_32x32x16_f16 v[18:33], v[6:9], v[126:129], 0
	s_nop 10
	v_cvt_pk_f16_f32 v13, v40, v41
	v_cvt_pk_f16_f32 v12, v38, v39
	v_cvt_pk_f16_f32 v11, v36, v37
	v_cvt_pk_f16_f32 v10, v34, v35
	v_cvt_pk_f16_f32 v17, v48, v49
	v_cvt_pk_f16_f32 v16, v46, v47
	v_cvt_pk_f16_f32 v15, v44, v45
	v_mfma_f32_32x32x16_f16 v[50:65], v[6:9], v[110:113], 0
	v_bitop3_b32 v6, v171, s27, v170 bitop3:0x36
	v_cvt_pk_f16_f32 v14, v42, v43
	v_mfma_f32_32x32x16_f16 v[18:33], v[2:5], v[122:125], v[18:33]
	s_waitcnt vmcnt(12)
	v_mfma_f32_32x32x16_f16 v[50:65], v[2:5], v[106:109], v[50:65]
	ds_read_b128 v[2:5], v6
	ds_read_b128 v[6:9], v6 offset:32768
	v_mfma_f32_32x32x16_f16 v[18:33], v[10:13], v[118:121], v[18:33]
	s_waitcnt vmcnt(11)
	v_mfma_f32_32x32x16_f16 v[50:65], v[10:13], v[94:97], v[50:65]
	s_waitcnt vmcnt(7) lgkmcnt(1)
	v_mfma_f32_32x32x16_f16 v[34:49], v[2:5], v[66:69], 0
	v_mfma_f32_32x32x16_f16 v[18:33], v[14:17], v[114:117], v[18:33]
	v_mfma_f32_32x32x16_f16 v[50:65], v[14:17], v[90:93], v[50:65]
	v_bitop3_b32 v14, v171, s26, v170 bitop3:0x36
	ds_read_b128 v[10:13], v14
	ds_read_b128 v[14:17], v14 offset:32768
	s_nop 7
	v_cvt_pk_f16_f32 v25, v24, v25
	v_cvt_pk_f16_f32 v24, v22, v23
	v_cvt_pk_f16_f32 v23, v20, v21
	v_cvt_pk_f16_f32 v22, v18, v19
	v_cvt_pk_f16_f32 v21, v32, v33
	s_waitcnt vmcnt(6) lgkmcnt(1)
	v_mfma_f32_32x32x16_f16 v[34:49], v[10:13], v[70:73], v[34:49]
	v_cvt_pk_f16_f32 v20, v30, v31
	v_cvt_pk_f16_f32 v19, v28, v29
	v_cvt_pk_f16_f32 v18, v26, v27
	ds_write_b128 v173, v[22:25]
	ds_write_b128 v172, v[18:21]
	v_cvt_pk_f16_f32 v21, v56, v57
	v_cvt_pk_f16_f32 v20, v54, v55
	s_waitcnt vmcnt(5)
	v_mfma_f32_32x32x16_f16 v[34:49], v[6:9], v[74:77], v[34:49]
	v_cvt_pk_f16_f32 v19, v52, v53
	v_cvt_pk_f16_f32 v18, v50, v51
	ds_write_b128 v173, v[18:21] offset:32768
	v_cvt_pk_f16_f32 v21, v64, v65
	v_cvt_pk_f16_f32 v20, v62, v63
	v_cvt_pk_f16_f32 v19, v60, v61
	v_cvt_pk_f16_f32 v18, v58, v59
	s_waitcnt vmcnt(4) lgkmcnt(3)
	v_mfma_f32_32x32x16_f16 v[34:49], v[14:17], v[78:81], v[34:49]
	ds_write_b128 v172, v[18:21] offset:32768
	s_waitcnt vmcnt(3)
	v_mfma_f32_32x32x16_f16 v[66:81], v[2:5], v[82:85], 0
	s_nop 8
	v_cvt_pk_f16_f32 v41, v40, v41
	v_cvt_pk_f16_f32 v40, v38, v39
	v_cvt_pk_f16_f32 v39, v36, v37
	v_cvt_pk_f16_f32 v38, v34, v35
	v_cvt_pk_f16_f32 v85, v48, v49
	v_cvt_pk_f16_f32 v84, v46, v47
	v_cvt_pk_f16_f32 v83, v44, v45
	s_waitcnt vmcnt(2)
	v_mfma_f32_32x32x16_f16 v[66:81], v[10:13], v[86:89], v[66:81]
	v_cvt_pk_f16_f32 v82, v42, v43
	s_waitcnt vmcnt(1)
	v_mfma_f32_32x32x16_f16 v[66:81], v[6:9], v[182:185], v[66:81]
	s_waitcnt vmcnt(0)
	v_mfma_f32_32x32x16_f16 v[66:81], v[14:17], v[186:189], v[66:81]
	v_mfma_f32_32x32x16_f16 v[2:17], v[38:41], v[126:129], 0
	s_nop 10
	v_cvt_pk_f16_f32 v73, v72, v73
	v_cvt_pk_f16_f32 v72, v70, v71
	v_cvt_pk_f16_f32 v70, v66, v67
	v_cvt_pk_f16_f32 v67, v76, v77
	v_cvt_pk_f16_f32 v66, v74, v75
	global_load_dwordx4 v[74:77], v154, s[2:3]
	v_cvt_pk_f16_f32 v71, v68, v69
	v_cvt_pk_f16_f32 v69, v80, v81
	v_cvt_pk_f16_f32 v68, v78, v79
	global_load_dwordx4 v[78:81], v154, s[2:3] offset:1024
	ds_read_b128 v[18:21], v180
	ds_read_b128 v[22:25], v176
	ds_read_b128 v[26:29], v180 offset:32768
	global_load_dwordx4 v[30:33], v154, s[2:3] offset:2048
	v_mfma_f32_32x32x16_f16 v[34:49], v[38:41], v[110:113], 0
	v_mfma_f32_32x32x16_f16 v[2:17], v[82:85], v[122:125], v[2:17]
	v_mfma_f32_32x32x16_f16 v[34:49], v[82:85], v[106:109], v[34:49]
	ds_read_b128 v[82:85], v176 offset:32768
	s_waitcnt vmcnt(2) lgkmcnt(3)
	v_mfma_f32_32x32x16_f16 v[50:65], v[18:21], v[74:77], 0
	v_mfma_f32_32x32x16_f16 v[2:17], v[70:73], v[118:121], v[2:17]
	v_mfma_f32_32x32x16_f16 v[34:49], v[70:73], v[94:97], v[34:49]
	v_lshl_add_u64 v[70:71], s[2:3], 0, v[154:155]
	v_add_co_u32_e32 v152, vcc, s23, v70
	s_nop 1
	v_addc_co_u32_e32 v153, vcc, 0, v71, vcc
	s_waitcnt vmcnt(1) lgkmcnt(2)
	v_mfma_f32_32x32x16_f16 v[50:65], v[22:25], v[78:81], v[50:65]
	v_mfma_f32_32x32x16_f16 v[2:17], v[66:69], v[114:117], v[2:17]
	v_mfma_f32_32x32x16_f16 v[34:49], v[66:69], v[90:93], v[34:49]
	global_load_dwordx4 v[66:69], v154, s[2:3] offset:3072
	s_nop 9
	v_cvt_pk_f16_f32 v9, v8, v9
	v_cvt_pk_f16_f32 v8, v6, v7
	v_cvt_pk_f16_f32 v7, v4, v5
	v_cvt_pk_f16_f32 v6, v2, v3
	v_cvt_pk_f16_f32 v5, v16, v17
	v_cvt_pk_f16_f32 v4, v14, v15
	s_waitcnt vmcnt(1) lgkmcnt(1)
	v_mfma_f32_32x32x16_f16 v[50:65], v[26:29], v[30:33], v[50:65]
	global_load_dwordx4 v[30:33], v168, s[2:3]
	global_load_dwordx4 v[86:89], v[152:153], off offset:1024
	s_nop 0
	global_load_dwordx4 v[168:171], v168, s[0:1]
	v_cvt_pk_f16_f32 v3, v12, v13
	v_cvt_pk_f16_f32 v2, v10, v11
	ds_write_b128 v175, v[6:9]
	ds_write_b128 v174, v[2:5]
	v_cvt_pk_f16_f32 v5, v40, v41
	s_waitcnt vmcnt(3) lgkmcnt(2)
	v_mfma_f32_32x32x16_f16 v[50:65], v[82:85], v[66:69], v[50:65]
	global_load_dwordx4 v[182:185], v154, s[0:1] offset:1024
	v_cvt_pk_f16_f32 v4, v38, v39
	v_cvt_pk_f16_f32 v3, v36, v37
	v_cvt_pk_f16_f32 v2, v34, v35
	ds_write_b128 v175, v[2:5] offset:32768
	v_cvt_pk_f16_f32 v5, v48, v49
	v_cvt_pk_f16_f32 v4, v46, v47
	s_waitcnt vmcnt(3)
	v_mfma_f32_32x32x16_f16 v[66:81], v[18:21], v[30:33], 0
	global_load_dwordx4 v[18:21], v[152:153], off offset:2048
	v_cvt_pk_f16_f32 v3, v44, v45
	v_cvt_pk_f16_f32 v2, v42, v43
	ds_write_b128 v174, v[2:5] offset:32768
	v_cvt_pk_f16_f32 v57, v56, v57
	v_cvt_pk_f16_f32 v56, v54, v55
	v_cvt_pk_f16_f32 v55, v52, v53
	s_waitcnt vmcnt(3)
	v_mfma_f32_32x32x16_f16 v[66:81], v[22:25], v[86:89], v[66:81]
	global_load_dwordx4 v[22:25], v[152:153], off offset:3072
	v_cvt_pk_f16_f32 v54, v50, v51
	s_waitcnt vmcnt(1)
	v_mfma_f32_32x32x16_f16 v[66:81], v[26:29], v[18:21], v[66:81]
	v_lshl_add_u64 v[18:19], s[0:1], 0, v[154:155]
	v_add_co_u32_e32 v152, vcc, s23, v18
	s_nop 1
	v_addc_co_u32_e32 v153, vcc, 0, v19, vcc
	global_load_dwordx4 v[86:89], v[152:153], off offset:1024
	s_waitcnt vmcnt(1)
	v_mfma_f32_32x32x16_f16 v[66:81], v[82:85], v[22:25], v[66:81]
	v_cvt_pk_f16_f32 v85, v64, v65
	v_cvt_pk_f16_f32 v84, v62, v63
	v_cvt_pk_f16_f32 v83, v60, v61
	v_cvt_pk_f16_f32 v82, v58, v59
	v_mfma_f32_32x32x16_f16 v[18:33], v[54:57], v[126:129], 0
	s_nop 6
	v_cvt_pk_f16_f32 v73, v72, v73
	v_cvt_pk_f16_f32 v72, v70, v71
	v_cvt_pk_f16_f32 v70, v66, v67
	v_cvt_pk_f16_f32 v67, v76, v77
	v_cvt_pk_f16_f32 v66, v74, v75
	global_load_dwordx4 v[74:77], v154, s[0:1]
	ds_read_b128 v[2:5], v181
	ds_read_b128 v[6:9], v177
	ds_read_b128 v[10:13], v181 offset:32768
	global_load_dwordx4 v[14:17], v154, s[0:1] offset:2048
	global_load_dwordx4 v[34:37], v154, s[0:1] offset:3072
	v_mfma_f32_32x32x16_f16 v[50:65], v[54:57], v[110:113], 0
	v_cvt_pk_f16_f32 v71, v68, v69
	v_cvt_pk_f16_f32 v69, v80, v81
	v_cvt_pk_f16_f32 v68, v78, v79
	v_mfma_f32_32x32x16_f16 v[18:33], v[82:85], v[122:125], v[18:33]
	v_mfma_f32_32x32x16_f16 v[50:65], v[82:85], v[106:109], v[50:65]
	ds_read_b128 v[82:85], v177 offset:32768
	v_mfma_f32_32x32x16_f16 v[18:33], v[70:73], v[118:121], v[18:33]
	v_mfma_f32_32x32x16_f16 v[50:65], v[70:73], v[94:97], v[50:65]
	v_mfma_f32_32x32x16_f16 v[18:33], v[66:69], v[114:117], v[18:33]
	v_mfma_f32_32x32x16_f16 v[50:65], v[66:69], v[90:93], v[50:65]
	s_nop 10
	v_cvt_pk_f16_f32 v25, v24, v25
	v_cvt_pk_f16_f32 v24, v22, v23
	v_cvt_pk_f16_f32 v23, v20, v21
	v_cvt_pk_f16_f32 v22, v18, v19
	ds_write_b128 v132, v[22:25]
	s_waitcnt vmcnt(2) lgkmcnt(4)
	v_mfma_f32_32x32x16_f16 v[66:81], v[2:5], v[74:77], 0
	s_waitcnt lgkmcnt(3)
	v_mfma_f32_32x32x16_f16 v[66:81], v[6:9], v[182:185], v[66:81]
	s_waitcnt vmcnt(1) lgkmcnt(2)
	v_mfma_f32_32x32x16_f16 v[66:81], v[10:13], v[14:17], v[66:81]
	s_waitcnt vmcnt(0) lgkmcnt(1)
	v_mfma_f32_32x32x16_f16 v[66:81], v[82:85], v[34:37], v[66:81]
	v_mfma_f32_32x32x16_f16 v[34:49], v[2:5], v[168:171], 0
	global_load_dwordx4 v[2:5], v[152:153], off offset:2048
	s_nop 9
	v_cvt_pk_f16_f32 v73, v72, v73
	v_cvt_pk_f16_f32 v72, v70, v71
	v_cvt_pk_f16_f32 v71, v68, v69
	v_cvt_pk_f16_f32 v70, v66, v67
	v_cvt_pk_f16_f32 v69, v80, v81
	v_cvt_pk_f16_f32 v68, v78, v79
	v_mfma_f32_32x32x16_f16 v[34:49], v[6:9], v[86:89], v[34:49]
	global_load_dwordx4 v[6:9], v[152:153], off offset:3072
	v_cvt_pk_f16_f32 v67, v76, v77
	v_cvt_pk_f16_f32 v66, v74, v75
	s_waitcnt vmcnt(1)
	v_mfma_f32_32x32x16_f16 v[34:49], v[10:13], v[2:5], v[34:49]
	s_waitcnt vmcnt(0)
	v_mfma_f32_32x32x16_f16 v[34:49], v[82:85], v[6:9], v[34:49]
	v_mfma_f32_32x32x16_f16 v[2:17], v[70:73], v[126:129], 0
	s_nop 10
	v_cvt_pk_f16_f32 v41, v40, v41
	v_cvt_pk_f16_f32 v40, v38, v39
	v_cvt_pk_f16_f32 v38, v34, v35
	v_cvt_pk_f16_f32 v35, v44, v45
	v_cvt_pk_f16_f32 v34, v42, v43
	v_cvt_pk_f16_f32 v45, v32, v33
	v_cvt_pk_f16_f32 v44, v30, v31
	v_cvt_pk_f16_f32 v43, v28, v29
	v_cvt_pk_f16_f32 v42, v26, v27
	v_mfma_f32_32x32x16_f16 v[18:33], v[70:73], v[110:113], 0
	v_cvt_pk_f16_f32 v39, v36, v37
	v_cvt_pk_f16_f32 v37, v48, v49
	v_cvt_pk_f16_f32 v36, v46, v47
	ds_write_b128 v131, v[42:45]
	v_cvt_pk_f16_f32 v45, v56, v57
	v_cvt_pk_f16_f32 v44, v54, v55
	v_cvt_pk_f16_f32 v43, v52, v53
	v_mfma_f32_32x32x16_f16 v[2:17], v[66:69], v[122:125], v[2:17]
	v_cvt_pk_f16_f32 v42, v50, v51
	ds_write_b128 v132, v[42:45] offset:32768
	v_cvt_pk_f16_f32 v45, v64, v65
	v_cvt_pk_f16_f32 v44, v62, v63
	v_cvt_pk_f16_f32 v43, v60, v61
	v_cvt_pk_f16_f32 v42, v58, v59
	ds_write_b128 v131, v[42:45] offset:32768
	v_mfma_f32_32x32x16_f16 v[18:33], v[66:69], v[106:109], v[18:33]
	v_mfma_f32_32x32x16_f16 v[2:17], v[38:41], v[118:121], v[2:17]
	v_mfma_f32_32x32x16_f16 v[18:33], v[38:41], v[94:97], v[18:33]
	v_mfma_f32_32x32x16_f16 v[2:17], v[34:37], v[114:117], v[2:17]
	v_mfma_f32_32x32x16_f16 v[18:33], v[34:37], v[90:93], v[18:33]
	s_nop 10
	v_cvt_pk_f16_f32 v9, v8, v9
	v_cvt_pk_f16_f32 v8, v6, v7
	v_cvt_pk_f16_f32 v7, v4, v5
	v_cvt_pk_f16_f32 v6, v2, v3
	v_cvt_pk_f16_f32 v5, v16, v17
	v_cvt_pk_f16_f32 v4, v14, v15
	v_cvt_pk_f16_f32 v3, v12, v13
	v_cvt_pk_f16_f32 v2, v10, v11
	ds_write_b128 v135, v[6:9]
	ds_write_b128 v133, v[2:5]
	v_cvt_pk_f16_f32 v5, v24, v25
	v_cvt_pk_f16_f32 v4, v22, v23
	v_cvt_pk_f16_f32 v3, v20, v21
	v_cvt_pk_f16_f32 v2, v18, v19
	ds_write_b128 v135, v[2:5] offset:32768
	v_cvt_pk_f16_f32 v5, v32, v33
	v_cvt_pk_f16_f32 v4, v30, v31
	v_cvt_pk_f16_f32 v3, v28, v29
	v_cvt_pk_f16_f32 v2, v26, v27
	ds_write_b128 v133, v[2:5] offset:32768
	s_cmp_eq_u32 s35, 0
	s_cbranch_scc1 .Lprio4_old
	s_setprio 1
	s_branch .Lprio4_done

.Lprio4_done:
	s_waitcnt lgkmcnt(0)
	s_barrier
	s_cmp_lt_i32 s22, 0
	s_cbranch_scc0 .Lno_pref
	s_add_u32 s36, s10, 0x140000
	s_addc_u32 s37, s11, 0
	v_lshlrev_b32_e32 v192, 3, v156
	v_lshlrev_b32_e32 v193, 3, v167
	global_load_dwordx2 v[190:191], v192, s[36:37]
	global_load_dwordx2 v[194:195], v193, s[36:37] offset:2048
